# speedup vs baseline: 1.0102x; 1.0102x over previous
.Lp_q:
	v_lshrrev_b32_e32 v122, 5, v0
	v_lshlrev_b32_e32 v122, 10, v122
	v_and_b32_e32 v125, 31, v0
	v_lshl_add_u32 v122, v125, 4, v122
	s_add_u32 s76, s38, 0x2000
	s_addc_u32 s77, s39, 0
	global_load_dwordx4 v[44:47], v120, s[76:77] nt
	s_and_b32 s13, s2, 7
	s_lshl_b32 s14, s13, 14
	v_add_u32_e32 v125, s14, v122
	global_load_dwordx4 v[132:135], v125, s[28:29]
	s_add_i32 s13, s2, 1
	s_and_b32 s13, s13, 7
	s_lshl_b32 s14, s13, 14
	v_add_u32_e32 v125, s14, v122
	global_load_dwordx4 v[136:139], v125, s[28:29]
	s_add_i32 s13, s2, 2
	s_and_b32 s13, s13, 7
	s_lshl_b32 s14, s13, 14
	v_add_u32_e32 v125, s14, v122
	global_load_dwordx4 v[140:143], v125, s[28:29]
	s_add_i32 s13, s2, 3
	s_and_b32 s13, s13, 7
	s_lshl_b32 s14, s13, 14
	v_add_u32_e32 v125, s14, v122
	global_load_dwordx4 v[144:147], v125, s[28:29]
	s_add_i32 s13, s2, 4
	s_and_b32 s13, s13, 7
	s_lshl_b32 s14, s13, 14
	v_add_u32_e32 v125, s14, v122
	global_load_dwordx4 v[148:151], v125, s[28:29]
	s_add_i32 s13, s2, 5
	s_and_b32 s13, s13, 7
	s_lshl_b32 s14, s13, 14
	v_add_u32_e32 v125, s14, v122
	global_load_dwordx4 v[152:155], v125, s[28:29]
	s_add_i32 s13, s2, 6
	s_and_b32 s13, s13, 7
	s_lshl_b32 s14, s13, 14
	v_add_u32_e32 v125, s14, v122
	global_load_dwordx4 v[156:159], v125, s[28:29]
	s_add_i32 s13, s2, 7
	s_and_b32 s13, s13, 7
	s_lshl_b32 s14, s13, 14
	v_add_u32_e32 v125, s14, v122
	global_load_dwordx4 v[160:163], v125, s[28:29]
	s_mov_b64 s[72:73], s[0:1]
	s_mov_b32 s74, s2
	v_mov_b32_e32 v131, v0
	v_add_u32_e32 v116, 0x11000, v52
	v_add_u32_e32 v117, 0x12100, v52
	v_add_u32_e32 v118, v27, v25
	v_add_u32_e32 v118, 0x12100, v118
	v_add_u32_e32 v119, 0x11000, v58
	s_waitcnt vmcnt(19)
	v_cvt_pk_bf16_f32 v12, v2, v3
	v_cvt_pk_bf16_f32 v13, v4, v5
	ds_write_b64 v124, v[12:13]
	s_waitcnt vmcnt(18)
	v_cvt_pk_bf16_f32 v6, v80, v81
	v_cvt_pk_bf16_f32 v7, v82, v83
	s_and_b32 s13, s2, 7
	s_mul_i32 s14, s13, 0x1100
	v_add_u32_e32 v125, s14, v58
	ds_write_b64 v125, v[6:7]
	s_waitcnt vmcnt(17)
	v_cvt_pk_bf16_f32 v8, v84, v85
	v_cvt_pk_bf16_f32 v9, v86, v87
	s_add_i32 s13, s2, 1
	s_and_b32 s13, s13, 7
	s_mul_i32 s14, s13, 0x1100
	v_add_u32_e32 v10, s14, v58
	ds_write_b64 v10, v[8:9]
	s_waitcnt vmcnt(16)
	v_cvt_pk_bf16_f32 v6, v88, v89
	v_cvt_pk_bf16_f32 v7, v90, v91
	s_add_i32 s13, s2, 2
	s_and_b32 s13, s13, 7
	s_mul_i32 s14, s13, 0x1100
	v_add_u32_e32 v125, s14, v58
	ds_write_b64 v125, v[6:7]
	s_waitcnt vmcnt(15)
	v_cvt_pk_bf16_f32 v8, v92, v93
	v_cvt_pk_bf16_f32 v9, v94, v95
	s_add_i32 s13, s2, 3
	s_and_b32 s13, s13, 7
	s_mul_i32 s14, s13, 0x1100
	v_add_u32_e32 v10, s14, v58
	ds_write_b64 v10, v[8:9]
	s_waitcnt vmcnt(14)
	v_cvt_pk_bf16_f32 v6, v96, v97
	v_cvt_pk_bf16_f32 v7, v98, v99
	s_add_i32 s13, s2, 4
	s_and_b32 s13, s13, 7
	s_mul_i32 s14, s13, 0x1100
	v_add_u32_e32 v125, s14, v58
	ds_write_b64 v125, v[6:7]
	s_waitcnt vmcnt(13)
	v_cvt_pk_bf16_f32 v8, v100, v101
	v_cvt_pk_bf16_f32 v9, v102, v103
	s_add_i32 s13, s2, 5
	s_and_b32 s13, s13, 7
	s_mul_i32 s14, s13, 0x1100
	v_add_u32_e32 v10, s14, v58
	ds_write_b64 v10, v[8:9]
	s_waitcnt vmcnt(12)
	v_cvt_pk_bf16_f32 v6, v108, v109
	v_cvt_pk_bf16_f32 v7, v110, v111
	s_add_i32 s13, s2, 6
	s_and_b32 s13, s13, 7
	s_mul_i32 s14, s13, 0x1100
	v_add_u32_e32 v125, s14, v58
	ds_write_b64 v125, v[6:7]
	s_waitcnt vmcnt(11)
	v_cvt_pk_bf16_f32 v8, v112, v113
	v_cvt_pk_bf16_f32 v9, v114, v115
	s_add_i32 s13, s2, 7
	s_and_b32 s13, s13, 7
	s_mul_i32 s14, s13, 0x1100
	v_add_u32_e32 v10, s14, v58
	ds_write_b64 v10, v[8:9]
	s_waitcnt vmcnt(7)
	v_cvt_pk_bf16_f32 v6, v132, v133
	v_cvt_pk_bf16_f32 v7, v134, v135
	s_and_b32 s13, s2, 7
	s_mul_i32 s14, s13, 0x1100
	s_add_i32 s14, s14, 34816
	v_add_u32_e32 v125, s14, v58
	ds_write_b64 v125, v[6:7]
	s_waitcnt vmcnt(6)
	v_cvt_pk_bf16_f32 v8, v136, v137
	v_cvt_pk_bf16_f32 v9, v138, v139
	s_add_i32 s13, s2, 1
	s_and_b32 s13, s13, 7
	s_mul_i32 s14, s13, 0x1100
	s_add_i32 s14, s14, 34816
	v_add_u32_e32 v10, s14, v58
	ds_write_b64 v10, v[8:9]
	s_waitcnt vmcnt(5)
	v_cvt_pk_bf16_f32 v6, v140, v141
	v_cvt_pk_bf16_f32 v7, v142, v143
	s_add_i32 s13, s2, 2
	s_and_b32 s13, s13, 7
	s_mul_i32 s14, s13, 0x1100
	s_add_i32 s14, s14, 34816
	v_add_u32_e32 v125, s14, v58
	ds_write_b64 v125, v[6:7]
	s_waitcnt vmcnt(4)
	v_cvt_pk_bf16_f32 v8, v144, v145
	v_cvt_pk_bf16_f32 v9, v146, v147
	s_add_i32 s13, s2, 3
	s_and_b32 s13, s13, 7
	s_mul_i32 s14, s13, 0x1100
	s_add_i32 s14, s14, 34816
	v_add_u32_e32 v10, s14, v58
	ds_write_b64 v10, v[8:9]
	s_waitcnt vmcnt(3)
	v_cvt_pk_bf16_f32 v6, v148, v149
	v_cvt_pk_bf16_f32 v7, v150, v151
	s_add_i32 s13, s2, 4
	s_and_b32 s13, s13, 7
	s_mul_i32 s14, s13, 0x1100
	s_add_i32 s14, s14, 34816
	v_add_u32_e32 v125, s14, v58
	ds_write_b64 v125, v[6:7]
	s_waitcnt vmcnt(2)
	v_cvt_pk_bf16_f32 v8, v152, v153
	v_cvt_pk_bf16_f32 v9, v154, v155
	s_add_i32 s13, s2, 5
	s_and_b32 s13, s13, 7
	s_mul_i32 s14, s13, 0x1100
	s_add_i32 s14, s14, 34816
	v_add_u32_e32 v10, s14, v58
	ds_write_b64 v10, v[8:9]
	s_waitcnt vmcnt(1)
	v_cvt_pk_bf16_f32 v6, v156, v157
	v_cvt_pk_bf16_f32 v7, v158, v159
	s_add_i32 s13, s2, 6
	s_and_b32 s13, s13, 7
	s_mul_i32 s14, s13, 0x1100
	s_add_i32 s14, s14, 34816
	v_add_u32_e32 v125, s14, v58
	ds_write_b64 v125, v[6:7]
	s_waitcnt vmcnt(0)
	v_cvt_pk_bf16_f32 v8, v160, v161
	v_cvt_pk_bf16_f32 v9, v162, v163
	s_add_i32 s13, s2, 7
	s_and_b32 s13, s13, 7
	s_mul_i32 s14, s13, 0x1100
	s_add_i32 s14, s14, 34816
	v_add_u32_e32 v10, s14, v58
	ds_write_b64 v10, v[8:9]
	v_cvt_pk_bf16_f32 v12, v44, v45
	v_cvt_pk_bf16_f32 v13, v46, v47
	ds_write_b64 v119, v[12:13]
	s_lshl_b32 s2, s74, 1
	s_lshl_b32 s12, s2, 4
	s_waitcnt lgkmcnt(0)
	s_barrier
	ds_read_b128 v[60:63], v56
	ds_read_b128 v[28:31], v53
	ds_read_b128 v[80:83], v116
	ds_read_b128 v[64:67], v56 offset:64
	ds_read_b128 v[32:35], v53 offset:64
	ds_read_b128 v[84:87], v116 offset:64
	ds_read_b128 v[68:71], v56 offset:128
	ds_read_b128 v[36:39], v53 offset:128
	ds_read_b128 v[88:91], v116 offset:128
	ds_read_b128 v[72:75], v56 offset:192
	ds_read_b128 v[40:43], v53 offset:192
	ds_read_b128 v[92:95], v116 offset:192
	s_waitcnt lgkmcnt(9)
	v_mfma_f32_16x16x32_bf16 v[18:21], v[28:31], v[60:63], 0
	v_mfma_f32_16x16x32_bf16 v[96:99], v[80:83], v[60:63], 0
	s_waitcnt lgkmcnt(6)
	v_mfma_f32_16x16x32_bf16 v[18:21], v[32:35], v[64:67], v[18:21]
	v_mfma_f32_16x16x32_bf16 v[96:99], v[84:87], v[64:67], v[96:99]
	s_waitcnt lgkmcnt(3)
	v_mfma_f32_16x16x32_bf16 v[18:21], v[36:39], v[68:71], v[18:21]
	v_mfma_f32_16x16x32_bf16 v[96:99], v[88:91], v[68:71], v[96:99]
	s_waitcnt lgkmcnt(0)
	v_mfma_f32_16x16x32_bf16 v[18:21], v[40:43], v[72:75], v[18:21]
	v_mfma_f32_16x16x32_bf16 v[96:99], v[92:95], v[72:75], v[96:99]
	s_nop 7
	v_mul_f32_e32 v18, s44, v18
	v_mul_f32_e32 v19, s44, v19
	v_mul_f32_e32 v20, s44, v20
	v_mul_f32_e32 v21, s44, v21
	v_mul_f32_e32 v96, s44, v96
	v_mul_f32_e32 v97, s44, v97
	v_mul_f32_e32 v98, s44, v98
	v_mul_f32_e32 v99, s44, v99
	v_cvt_pk_bf16_f32 v18, v18, v18
	v_cvt_pk_bf16_f32 v19, v19, v19
	v_cvt_pk_bf16_f32 v20, v20, v20
	v_cvt_pk_bf16_f32 v21, v21, v21
	v_cvt_pk_bf16_f32 v96, v96, v96
	v_cvt_pk_bf16_f32 v97, v97, v97
	v_cvt_pk_bf16_f32 v98, v98, v98
	v_cvt_pk_bf16_f32 v99, v99, v99
	ds_write_b16 v55, v18
	ds_write_b16 v55, v19 offset:272
	ds_write_b16 v55, v20 offset:544
	ds_write_b16 v55, v21 offset:816
	ds_write_b16 v118, v96
	ds_write_b16 v118, v97 offset:272
	ds_write_b16 v118, v98 offset:544
	ds_write_b16 v118, v99 offset:816
	s_waitcnt lgkmcnt(0)
	s_barrier
	ds_read_b128 v[60:63], v57
	ds_read_b128 v[28:31], v54
	ds_read_b128 v[80:83], v117
	ds_read_b128 v[64:67], v57 offset:64
	ds_read_b128 v[32:35], v54 offset:64
	ds_read_b128 v[84:87], v117 offset:64
	ds_read_b128 v[68:71], v57 offset:128
	ds_read_b128 v[36:39], v54 offset:128
	ds_read_b128 v[88:91], v117 offset:128
	ds_read_b128 v[72:75], v57 offset:192
	ds_read_b128 v[40:43], v54 offset:192
	ds_read_b128 v[92:95], v117 offset:192
	s_waitcnt lgkmcnt(9)
	v_mfma_f32_16x16x32_bf16 v[18:21], v[28:31], v[60:63], 0
	v_mfma_f32_16x16x32_bf16 v[96:99], v[80:83], v[60:63], 0
	s_waitcnt lgkmcnt(6)
	v_mfma_f32_16x16x32_bf16 v[18:21], v[32:35], v[64:67], v[18:21]
	v_mfma_f32_16x16x32_bf16 v[96:99], v[84:87], v[64:67], v[96:99]
	s_waitcnt lgkmcnt(3)
	v_mfma_f32_16x16x32_bf16 v[18:21], v[36:39], v[68:71], v[18:21]
	v_mfma_f32_16x16x32_bf16 v[96:99], v[88:91], v[68:71], v[96:99]
	s_waitcnt lgkmcnt(0)
	v_mfma_f32_16x16x32_bf16 v[18:21], v[40:43], v[72:75], v[18:21]
	v_mfma_f32_16x16x32_bf16 v[96:99], v[92:95], v[72:75], v[96:99]
	s_load_dwordx2 s[4:5], s[0:1], 0x68
	s_nop 4
	v_lshl_or_b32 v30, v24, 2, s12
	v_lshlrev_b32_e32 v30, 9, v30
	v_add_u32_e32 v30, v30, v106
	v_add_u32_e32 v31, 0x2000, v30
	v_add_u32_e32 v37, v27, v25
	v_add_u32_e32 v38, 0x13200, v37
	v_add_u32_e32 v37, 0x19200, v37
	s_waitcnt lgkmcnt(0)
	global_store_dword v30, v18, s[4:5] sc1
	global_store_dword v30, v19, s[4:5] offset:512 sc1
	global_store_dword v30, v20, s[4:5] offset:1024 sc1
	global_store_dword v30, v21, s[4:5] offset:1536 sc1
	global_store_dword v31, v96, s[4:5] sc1
	global_store_dword v31, v97, s[4:5] offset:512 sc1
	global_store_dword v31, v98, s[4:5] offset:1024 sc1
	global_store_dword v31, v99, s[4:5] offset:1536 sc1
	v_cvt_pk_bf16_f32 v100, v18, v18
	v_cvt_pk_bf16_f32 v101, v19, v19
	v_cvt_pk_bf16_f32 v102, v20, v20
	v_cvt_pk_bf16_f32 v103, v21, v21
	v_mul_f32_e32 v104, v18, v18
	v_mul_f32_e32 v105, v19, v19
	v_mul_f32_e32 v106, v20, v20
	v_mul_f32_e32 v107, v21, v21
	v_cvt_pk_bf16_f32 v108, v96, v96
	v_cvt_pk_bf16_f32 v109, v97, v97
	v_cvt_pk_bf16_f32 v110, v98, v98
	v_cvt_pk_bf16_f32 v111, v99, v99
	v_mul_f32_e32 v112, v96, v96
	v_mul_f32_e32 v113, v97, v97
	v_mul_f32_e32 v114, v98, v98
	v_mul_f32_e32 v115, v99, v99
	v_cvt_pk_bf16_f32 v104, v104, v104
	v_cvt_pk_bf16_f32 v105, v105, v105
	v_cvt_pk_bf16_f32 v106, v106, v106
	v_cvt_pk_bf16_f32 v107, v107, v107
	v_cvt_pk_bf16_f32 v112, v112, v112
	v_cvt_pk_bf16_f32 v113, v113, v113
	v_cvt_pk_bf16_f32 v114, v114, v114
	v_cvt_pk_bf16_f32 v115, v115, v115
	ds_write_b16 v37, v100
	ds_write_b16 v37, v101 offset:272
	ds_write_b16 v37, v102 offset:544
	ds_write_b16 v37, v103 offset:816
	ds_write_b16 v37, v104 offset:4352
	ds_write_b16 v37, v105 offset:4624
	ds_write_b16 v37, v106 offset:4896
	ds_write_b16 v37, v107 offset:5168
	ds_write_b16 v38, v108
	ds_write_b16 v38, v109 offset:272
	ds_write_b16 v38, v110 offset:544
	ds_write_b16 v38, v111 offset:816
	ds_write_b16 v38, v112 offset:4352
	ds_write_b16 v38, v113 offset:4624
	ds_write_b16 v38, v114 offset:4896
	ds_write_b16 v38, v115 offset:5168
	v_max3_f32 v40, |v18|, |v19|, |v20|
	v_max3_f32 v41, |v96|, |v97|, |v98|
	v_and_b32_e32 v43, 0x7fffffff, v129
	v_max_f32_e64 v40, v40, |v21|
	v_max_f32_e64 v41, v41, |v99|
	s_nop 0
	v_max_f32_dpp v40, v40, v40 quad_perm:[1,0,3,2] row_mask:0xf bank_mask:0xf
	v_max_f32_dpp v41, v41, v41 quad_perm:[1,0,3,2] row_mask:0xf bank_mask:0xf
	v_add_f32_dpp v43, v43, v43 quad_perm:[1,0,3,2] row_mask:0xf bank_mask:0xf
	s_nop 0
	v_max_f32_dpp v40, v40, v40 quad_perm:[2,3,0,1] row_mask:0xf bank_mask:0xf
	v_max_f32_dpp v41, v41, v41 quad_perm:[2,3,0,1] row_mask:0xf bank_mask:0xf
	v_add_f32_dpp v43, v43, v43 quad_perm:[2,3,0,1] row_mask:0xf bank_mask:0xf
	s_nop 0
	v_max_f32_dpp v40, v40, v40 row_half_mirror row_mask:0xf bank_mask:0xf
	v_max_f32_dpp v41, v41, v41 row_half_mirror row_mask:0xf bank_mask:0xf
	v_add_f32_dpp v43, v43, v43 row_half_mirror row_mask:0xf bank_mask:0xf
	s_nop 0
	v_max_f32_dpp v40, v40, v40 row_mirror row_mask:0xf bank_mask:0xf
	v_max_f32_dpp v41, v41, v41 row_mirror row_mask:0xf bank_mask:0xf
	v_add_f32_dpp v43, v43, v43 row_mirror row_mask:0xf bank_mask:0xf
	s_nop 0
	v_readlane_b32 s8, v40, 0
	v_readlane_b32 s9, v40, 16
	v_readlane_b32 s10, v40, 32
	v_readlane_b32 s11, v40, 48
	v_readlane_b32 s82, v41, 0
	v_readlane_b32 s83, v41, 16
	v_readlane_b32 s84, v41, 32
	v_readlane_b32 s85, v41, 48
	s_nop 1
	v_mov_b32_e32 v44, s8
	v_mov_b32_e32 v46, s82
	v_max_f32_e32 v44, s9, v44
	v_max_f32_e32 v46, s83, v46
	v_max_f32_e32 v44, s10, v44
	v_max_f32_e32 v46, s84, v46
	v_max_f32_e32 v44, s11, v44
	v_max_f32_e32 v46, s85, v46
	v_mov_b32_e32 v45, v43
	v_mov_b32_e32 v47, v43
	v_mov_b32_e32 v32, 0x1d800
	v_lshl_or_b32 v32, v128, 6, v32
	v_mov_b32_e32 v33, 0x15400
	v_lshl_or_b32 v33, v128, 6, v33
	v_cmp_eq_u32_e32 vcc, 0, v126
	s_and_saveexec_b64 s[86:87], vcc
	ds_write_b64 v32, v[44:45]
	ds_write_b64 v33, v[46:47]
	s_or_b64 exec, exec, s[86:87]
	s_waitcnt lgkmcnt(0)
	s_barrier
	v_cmp_eq_u32_e32 vcc, 0, v0
	s_and_saveexec_b64 s[6:7], vcc
	s_cbranch_execz .Lq0_37
	v_mov_b32_e32 v18, 0x1d800
	v_mov_b32_e32 v20, 0x1d840
	ds_read_b64 v[18:19], v18
	ds_read_b64 v[20:21], v20
	v_mov_b32_e32 v24, 0x1d880
	v_mov_b32_e32 v26, 0x1d8c0
	ds_read_b64 v[24:25], v24
	ds_read_b64 v[26:27], v26
	s_waitcnt lgkmcnt(0)
	v_max_f32_e32 v18, v18, v18
	v_max_f32_e32 v20, v20, v20
	v_max_f32_e32 v18, v18, v20
	v_add_f32_e32 v19, v19, v21
	v_add_f32_e32 v19, v19, v25
	v_max3_f32 v21, v18, v24, v26
	v_mov_b32_e32 v18, 0x1d900
	v_add_f32_e32 v30, v19, v27
	v_mov_b32_e32 v19, 0x1d940
	v_mov_b32_e32 v20, 0x1d980
	ds_read_b64 v[24:25], v18
	ds_read_b64 v[26:27], v19
	ds_read_b64 v[28:29], v20
	v_mov_b32_e32 v18, 0x1d9c0
	ds_read_b96 v[18:20], v18
	s_mov_b32 s10, 0x3b800000
	s_waitcnt lgkmcnt(2)
	v_max3_f32 v21, v21, v24, v26
	s_waitcnt lgkmcnt(0)
	v_add_f32_e32 v20, v30, v25
	s_mov_b32 s11, 0x3eaab368
	v_max3_f32 v24, v21, v28, v18
	v_mul_f32_e32 v25, v24, v24
	v_add_f32_e32 v20, v20, v27
	v_pk_mul_f32 v[26:27], v[24:25], s[10:11]
	v_add_f32_e32 v20, v20, v29
	v_mov_b32_e32 v28, v26
	v_mul_f32_e32 v21, 0x3ec51eb8, v25
	v_mov_b32_e32 v18, v19
	v_mov_b32_e32 v19, v26
	v_fmac_f32_e32 v28, v24, v27
	v_pk_add_f32 v[18:19], v[20:21], v[18:19]
	s_mov_b32 s3, 0x3a83126f
	v_mul_f32_e32 v20, v18, v28
	s_load_dwordx2 s[8:9], s[0:1], 0x78
	v_cmp_nge_f32_e32 vcc, s3, v20
	v_mul_f32_e32 v18, v18, v19
	s_and_b64 s[10:11], vcc, exec
	v_cmp_nge_f32_e32 vcc, s3, v18
	s_cselect_b32 s12, 3, 2
	s_and_b64 s[10:11], vcc, exec
	s_cselect_b32 s12, s12, 1
	s_ashr_i32 s3, s2, 31
	s_lshl_b64 s[10:11], s[2:3], 2
	s_waitcnt lgkmcnt(0)
	s_add_u32 s8, s8, s10
	s_addc_u32 s9, s9, s11
	v_mov_b32_e32 v18, 0
	v_mov_b32_e32 v19, s12
	global_store_dword v18, v19, s[8:9] sc1

.Lq0_39:
	s_or_b64 exec, exec, s[6:7]
	s_add_i32 s2, s2, 1
	s_mov_b64 s[0:1], s[72:73]
	v_mov_b32_e32 v0, v131
	v_and_b32_e32 v1, 15, v0
	v_cmp_eq_u32_e32 vcc, 0, v0
	s_and_saveexec_b64 s[6:7], vcc
	s_cbranch_execz .Lq1_37
	v_mov_b32_e32 v18, 0x15400
	v_mov_b32_e32 v20, 0x15440
	ds_read_b64 v[18:19], v18
	ds_read_b64 v[20:21], v20
	v_mov_b32_e32 v24, 0x15480
	v_mov_b32_e32 v26, 0x154c0
	ds_read_b64 v[24:25], v24
	ds_read_b64 v[26:27], v26
	s_waitcnt lgkmcnt(0)
	v_max_f32_e32 v18, v18, v18
	v_max_f32_e32 v20, v20, v20
	v_max_f32_e32 v18, v18, v20
	v_add_f32_e32 v19, v19, v21
	v_add_f32_e32 v19, v19, v25
	v_max3_f32 v21, v18, v24, v26
	v_mov_b32_e32 v18, 0x15500
	v_add_f32_e32 v30, v19, v27
	v_mov_b32_e32 v19, 0x15540
	v_mov_b32_e32 v20, 0x15580
	ds_read_b64 v[24:25], v18
	ds_read_b64 v[26:27], v19
	ds_read_b64 v[28:29], v20
	v_mov_b32_e32 v18, 0x155c0
	ds_read_b96 v[18:20], v18
	s_mov_b32 s10, 0x3b800000
	s_waitcnt lgkmcnt(2)
	v_max3_f32 v21, v21, v24, v26
	s_waitcnt lgkmcnt(0)
	v_add_f32_e32 v20, v30, v25
	s_mov_b32 s11, 0x3eaab368
	v_max3_f32 v24, v21, v28, v18
	v_mul_f32_e32 v25, v24, v24
	v_add_f32_e32 v20, v20, v27
	v_pk_mul_f32 v[26:27], v[24:25], s[10:11]
	v_add_f32_e32 v20, v20, v29
	v_mov_b32_e32 v28, v26
	v_mul_f32_e32 v21, 0x3ec51eb8, v25
	v_mov_b32_e32 v18, v19
	v_mov_b32_e32 v19, v26
	v_fmac_f32_e32 v28, v24, v27
	v_pk_add_f32 v[18:19], v[20:21], v[18:19]
	s_mov_b32 s3, 0x3a83126f
	v_mul_f32_e32 v20, v18, v28
	s_load_dwordx2 s[8:9], s[0:1], 0x78
	v_cmp_nge_f32_e32 vcc, s3, v20
	v_mul_f32_e32 v18, v18, v19
	s_and_b64 s[10:11], vcc, exec
	v_cmp_nge_f32_e32 vcc, s3, v18
	s_cselect_b32 s12, 3, 2
	s_and_b64 s[10:11], vcc, exec
	s_cselect_b32 s12, s12, 1
	s_ashr_i32 s3, s2, 31
	s_lshl_b64 s[10:11], s[2:3], 2
	s_waitcnt lgkmcnt(0)
	s_add_u32 s8, s8, s10
	s_addc_u32 s9, s9, s11
	v_mov_b32_e32 v18, 0
	v_mov_b32_e32 v19, s12
	global_store_dword v18, v19, s[8:9] sc1
.Lq1_37:
	s_or_b64 exec, exec, s[6:7]
	s_movk_i32 s3, 0x200
	v_cmp_gt_u32_e32 vcc, s3, v0
	s_and_saveexec_b64 s[6:7], vcc
	s_cbranch_execz .Lq1_39
	v_lshrrev_b32_e32 v18, 4, v0
	v_bfe_u32 v18, v18, 3, 1
	s_load_dwordx2 s[0:1], s[0:1], 0x50
	v_lshl_or_b32 v18, s2, 1, v18
	v_lshrrev_b32_e32 v21, 8, v0
	v_ashrrev_i32_e32 v19, 31, v18
	v_lshlrev_b32_e32 v24, 10, v21
	v_mov_b32_e32 v25, 0
	v_lshl_add_u64 v[18:19], v[18:19], 2, v[24:25]
	v_lshrrev_b32_e32 v24, 2, v1
	v_or_b32_e32 v18, v18, v24
	v_bfe_u32 v20, v0, 4, 4
	v_lshlrev_b64 v[18:19], 9, v[18:19]
	s_waitcnt lgkmcnt(0)
	v_lshl_add_u64 v[26:27], s[0:1], 0, v[18:19]
	v_mul_u32_u24_e32 v18, 0x110, v20
	s_movk_i32 s0, 0x1100
	v_mad_u32_u24 v18, v21, s0, v18
	v_lshlrev_b32_e32 v1, 4, v1
	s_mov_b32 s0, 0x13200
	v_add3_u32 v1, v18, v1, s0
	ds_read_b128 v[18:21], v1
	v_lshlrev_b32_e32 v24, 7, v0
	v_and_b32_e32 v24, 0x180, v24
	v_lshl_add_u64 v[26:27], v[26:27], 0, v[24:25]
	v_and_b32_e32 v24, 0x70, v0
	v_lshl_add_u64 v[0:1], v[26:27], 0, v[24:25]
	s_waitcnt lgkmcnt(0)
	global_store_dwordx4 v[0:1], v[18:21], off sc1
.Lq1_39:
	s_or_b64 exec, exec, s[6:7]
	s_endpgm
